# baseline (speedup 1.0000x reference)
.LBB0_17:
	v_mfma_f32_32x32x16_bf16 v[112:127], a[192:195], a[128:131], v[0:15]
	v_exp_f32_e32 v48, v48
	v_exp_f32_e32 v49, v49
	ds_read_b64_tr_b16 v[172:173], v215 offset:0
	v_cvt_pk_bf16_f32 v164, v128, v129
	v_exp_f32_e32 v50, v50
	v_exp_f32_e32 v51, v51
	v_mfma_f32_32x32x16_bf16 v[96:111], a[192:195], a[160:163], v[16:31]
	ds_read_b64_tr_b16 v[174:175], v215 offset:0x800
	v_cvt_pk_bf16_f32 v165, v130, v131
	v_mfma_f32_32x32x16_bf16 v[80:95], a[224:227], a[128:131], v[0:15]
	ds_read_b64_tr_b16 v[184:185], v215 offset:0x200
	v_exp_f32_e32 v239, v52
	v_exp_f32_e32 v240, v53
	v_cvt_pk_bf16_f32 v166, v132, v133
	v_mfma_f32_32x32x16_bf16 v[64:79], a[224:227], a[160:163], v[16:31]
	ds_read_b64_tr_b16 v[186:187], v215 offset:0xa00
	ds_read_b64_tr_b16 v[180:181], v215 offset:0x400
	v_exp_f32_e32 v241, v54
	v_exp_f32_e32 v242, v55
	v_cvt_pk_bf16_f32 v167, v134, v135
	v_exp_f32_e32 v227, v56
	v_exp_f32_e32 v228, v57
	v_mfma_f32_32x32x16_bf16 v[112:127], a[196:199], a[132:135], v[112:127]
	ds_read_b64_tr_b16 v[182:183], v215 offset:0xc00
	v_cvt_pk_bf16_f32 v128, v136, v137
	v_exp_f32_e32 v229, v58
	v_exp_f32_e32 v230, v59
	v_mfma_f32_32x32x16_bf16 v[96:111], a[196:199], a[164:167], v[96:111]
	ds_read_b64_tr_b16 v[188:189], v215 offset:0x600
	v_cvt_pk_bf16_f32 v129, v138, v139
	v_exp_f32_e32 v231, v60
	v_exp_f32_e32 v232, v61
	v_mfma_f32_32x32x16_bf16 v[80:95], a[228:231], a[132:135], v[80:95]
	ds_read_b64_tr_b16 v[190:191], v215 offset:0xe00
	v_cvt_pk_bf16_f32 v130, v140, v141
	v_mfma_f32_32x32x16_bf16 v[64:79], a[228:231], a[164:167], v[64:79]
	ds_read_b64_tr_b16 v[176:177], v215 offset:0x1000
	v_exp_f32_e32 v233, v62
	v_exp_f32_e32 v234, v63
	ds_read_b64_tr_b16 v[178:179], v215 offset:0x1800
	v_cvt_pk_bf16_f32 v131, v142, v143
	v_exp_f32_e32 v141, v32
	v_exp_f32_e32 v142, v33
	v_mfma_f32_32x32x16_bf16 v[112:127], a[200:203], a[136:139], v[112:127]
	ds_read_b64_tr_b16 v[168:169], v215 offset:0x1200
	v_cvt_pk_bf16_f32 v192, v144, v145
	v_exp_f32_e32 v143, v34
	v_mfma_f32_32x32x16_bf16 v[96:111], a[200:203], a[168:171], v[96:111]
	ds_read_b64_tr_b16 v[170:171], v215 offset:0x1a00
	v_exp_f32_e32 v243, v35
	v_cvt_pk_bf16_f32 v193, v146, v147
	v_mfma_f32_32x32x16_bf16 v[80:95], a[232:235], a[136:139], v[80:95]
	ds_read_b64_tr_b16 v[160:161], v215 offset:0x1400
	v_exp_f32_e32 v244, v36
	v_exp_f32_e32 v245, v37
	v_cvt_pk_bf16_f32 v194, v148, v149
	v_mfma_f32_32x32x16_bf16 v[64:79], a[232:235], a[168:171], v[64:79]
	ds_read_b64_tr_b16 v[162:163], v215 offset:0x1c00
	ds_read_b64_tr_b16 v[136:137], v215 offset:0x1600
	v_exp_f32_e32 v246, v38
	v_exp_f32_e32 v247, v39
	v_cvt_pk_bf16_f32 v195, v150, v151
	v_exp_f32_e32 v148, v40
	v_exp_f32_e32 v149, v41
	v_mfma_f32_32x32x16_bf16 v[112:127], a[204:207], a[140:143], v[112:127]
	ds_read_b64_tr_b16 v[138:139], v215 offset:0x1e00
	v_cvt_pk_bf16_f32 v144, v152, v153
	v_exp_f32_e32 v150, v42
	v_exp_f32_e32 v151, v43
	v_mfma_f32_32x32x16_bf16 v[96:111], a[204:207], a[172:175], v[96:111]
	ds_read_b64_tr_b16 v[132:133], v215 offset:0x2000
	v_cvt_pk_bf16_f32 v145, v154, v155
	v_exp_f32_e32 v152, v44
	v_exp_f32_e32 v153, v45
	v_mfma_f32_32x32x16_bf16 v[80:95], a[236:239], a[140:143], v[80:95]
	ds_read_b64_tr_b16 v[134:135], v215 offset:0x2800
	v_cvt_pk_bf16_f32 v146, v156, v157
	v_mfma_f32_32x32x16_bf16 v[64:79], a[236:239], a[172:175], v[64:79]
	ds_read_b64_tr_b16 v[60:61], v215 offset:0x2200
	v_exp_f32_e32 v154, v46
	v_exp_f32_e32 v155, v47
	ds_read_b64_tr_b16 v[62:63], v215 offset:0x2a00
	v_cvt_pk_bf16_f32 v147, v158, v159
	s_mov_b32 s0, s29
	v_mfma_f32_32x32x16_bf16 v[112:127], a[208:211], a[144:147], v[112:127]
	ds_read_b64_tr_b16 v[56:57], v215 offset:0x2400
	v_cvt_pk_bf16_f32 v52, v48, v49
	v_add_f32_e32 v32, v236, v48
	v_add_f32_e32 v33, v235, v49
	s_add_i32 s57, s58, s59
	s_and_b32 s57, s57, 0x7ffff
	s_mov_b32 s33, s57
	s_mov_b32 s1, s33
	v_mfma_f32_32x32x16_bf16 v[96:111], a[208:211], a[176:179], v[96:111]
	ds_read_b64_tr_b16 v[58:59], v215 offset:0x2c00
	v_cvt_pk_bf16_f32 v53, v50, v51
	v_add_f32_e32 v32, v32, v50
	v_add_f32_e32 v33, v33, v51
	s_mov_b32 s35, s20
	v_mfma_f32_32x32x16_bf16 v[80:95], a[240:243], a[144:147], v[80:95]
	ds_read_b64_tr_b16 v[48:49], v215 offset:0x2600
	v_cvt_pk_bf16_f32 v54, v239, v240
	v_add_f32_e32 v32, v32, v239
	v_add_f32_e32 v33, v33, v240
	s_add_i32 s36, s57, 0x400
	v_mfma_f32_32x32x16_bf16 v[64:79], a[240:243], a[176:179], v[64:79]
	ds_read_b64_tr_b16 v[50:51], v215 offset:0x2e00
	ds_read_b64_tr_b16 v[44:45], v215 offset:0x3000
	v_cvt_pk_bf16_f32 v55, v241, v242
	v_add_f32_e32 v32, v32, v241
	v_add_f32_e32 v33, v33, v242
	s_mov_b32 s37, s21
	v_mfma_f32_32x32x16_bf16 v[112:127], a[212:215], a[148:151], v[112:127]
	ds_read_b64_tr_b16 v[46:47], v215 offset:0x3800
	v_add_f32_e32 v32, v32, v227
	v_add_f32_e32 v33, v33, v228
	s_add_i32 s34, s57, 0x800
	s_mov_b32 s38, s34
	v_mfma_f32_32x32x16_bf16 v[96:111], a[212:215], a[180:183], v[96:111]
	ds_read_b64_tr_b16 v[40:41], v215 offset:0x3200
	v_add_f32_e32 v32, v32, v229
	v_add_f32_e32 v33, v33, v230
	s_mov_b32 s39, s22
	v_mfma_f32_32x32x16_bf16 v[80:95], a[244:247], a[148:151], v[80:95]
	ds_read_b64_tr_b16 v[42:43], v215 offset:0x3a00
	v_add_f32_e32 v32, v32, v231
	v_add_f32_e32 v33, v33, v232
	s_add_i32 s40, s57, 0xc00
	v_mfma_f32_32x32x16_bf16 v[64:79], a[244:247], a[180:183], v[64:79]
	ds_read_b64_tr_b16 v[36:37], v215 offset:0x3400
	ds_read_b64_tr_b16 v[38:39], v215 offset:0x3c00
	v_add_f32_e32 v156, v32, v233
	v_add_f32_e32 v157, v33, v234
	s_mov_b32 s41, s23
	v_mfma_f32_32x32x16_bf16 v[112:127], a[216:219], a[152:155], v[112:127]
	ds_read_b64_tr_b16 v[32:33], v215 offset:0x3600
	v_cvt_pk_bf16_f32 v140, v141, v142
	v_add_f32_e32 v158, v237, v141
	v_add_f32_e32 v142, v238, v142
	s_mov_b32 s42, s58
	v_mfma_f32_32x32x16_bf16 v[96:111], a[216:219], a[184:187], v[96:111]
	ds_read_b64_tr_b16 v[34:35], v215 offset:0x3e00
	v_cvt_pk_bf16_f32 v141, v143, v243
	v_add_f32_e32 v143, v158, v143
	v_add_f32_e32 v158, v142, v243
	v_mfma_f32_32x32x16_bf16 v[80:95], a[248:251], a[152:155], v[80:95]
	s_mov_b32 s43, s24
	v_cvt_pk_bf16_f32 v142, v244, v245
	v_add_f32_e32 v159, v143, v244
	v_add_f32_e32 v158, v158, v245
	v_mfma_f32_32x32x16_bf16 v[64:79], a[248:251], a[184:187], v[64:79]
	s_add_i32 s44, s58, 0x80
	v_cvt_pk_bf16_f32 v143, v246, v247
	v_add_f32_e32 v159, v159, v246
	v_add_f32_e32 v158, v158, v247
	v_mfma_f32_32x32x16_bf16 v[112:127], a[220:223], a[156:159], v[112:127]
	s_mov_b32 s45, s25
	v_add_f32_e32 v159, v159, v148
	v_add_f32_e32 v158, v158, v149
	v_mfma_f32_32x32x16_bf16 v[96:111], a[220:223], a[188:191], v[96:111]
	s_add_i32 s46, s58, 0x800
	v_add_f32_e32 v159, v159, v150
	v_add_f32_e32 v158, v158, v151
	v_mfma_f32_32x32x16_bf16 v[80:95], a[252:255], a[156:159], v[80:95]
	s_mov_b32 s47, s26
	v_add_f32_e32 v159, v159, v152
	v_add_f32_e32 v158, v158, v153
	v_mfma_f32_32x32x16_bf16 v[64:79], a[252:255], a[188:191], v[64:79]
	s_add_i32 s48, s58, 0x880
	v_add_f32_e32 v159, v159, v154
	v_add_f32_e32 v158, v158, v155
	v_add_f32_e32 v156, v156, v157
	s_waitcnt vmcnt(0) lgkmcnt(0)
	s_barrier
	s_mov_b32 m0, s0
	v_mfma_f32_32x32x16_bf16 a[0:15], v[172:175], v[164:167], a[0:15]
	buffer_load_dwordx4 v222, s[12:15], s1 offen lds
	s_mov_b32 m0, s35
	v_mfma_f32_32x32x16_bf16 a[16:31], v[172:175], v[192:195], a[16:31]
	buffer_load_dwordx4 v223, s[12:15], s36 offen lds
	ds_read_b128 a[192:195], v217 offset:0
	s_mov_b32 m0, s37
	v_mfma_f32_32x32x16_bf16 a[32:47], v[184:187], v[164:167], a[32:47]
	v_add_f32_e32 v225, v225, v156
	v_add_f32_e32 v156, v159, v158
	buffer_load_dwordx4 v222, s[12:15], s38 offen lds
	ds_read_b128 a[196:199], v199 offset:0
	s_mov_b32 m0, s39
	v_mfma_f32_32x32x16_bf16 a[48:63], v[184:187], v[192:195], a[48:63]
	buffer_load_dwordx4 v223, s[12:15], s40 offen lds
	ds_read_b128 a[200:203], v198 offset:0
	s_mov_b32 m0, s41
	v_mfma_f32_32x32x16_bf16 a[64:79], v[180:183], v[164:167], a[64:79]
	v_add_f32_e32 v226, v226, v156
	buffer_load_dwordx4 v196, s[4:7], s42 offen lds
	ds_read_b128 a[204:207], v197 offset:0
	s_mov_b32 m0, s43
	v_mfma_f32_32x32x16_bf16 a[80:95], v[180:183], v[192:195], a[80:95]
	buffer_load_dwordx4 v196, s[4:7], s44 offen lds
	ds_read_b128 a[208:211], v217 offset:128
	s_mov_b32 m0, s45
	v_mfma_f32_32x32x16_bf16 a[96:111], v[188:191], v[164:167], a[96:111]
	buffer_load_dwordx4 v196, s[4:7], s46 offen lds
	ds_read_b128 a[212:215], v199 offset:128
	s_mov_b32 m0, s47
	v_mfma_f32_32x32x16_bf16 a[112:127], v[188:191], v[192:195], a[112:127]
	buffer_load_dwordx4 v196, s[4:7], s48 offen lds
	ds_read_b128 a[216:219], v198 offset:128
	s_nop 0
	v_mfma_f32_32x32x16_bf16 a[0:15], v[176:179], v[128:131], a[0:15]
	ds_read_b128 a[220:223], v197 offset:128
	s_cmp_gt_u32 s27, 12
	s_cbranch_scc1 .Lka_done
	s_cmp_gt_u32 s27, 4
	s_cbranch_scc1 .Lka_single
	v_cvt_pk_bf16_f32 v248, v248, v249
	v_cvt_pk_bf16_f32 v249, v250, v251
	v_cvt_pk_bf16_f32 v250, v252, v253
	v_cvt_pk_bf16_f32 v251, v254, v255
	v_lshrrev_b32_e32 v252, 1, v208
	buffer_store_dwordx4 v[248:251], v252, s[12:15], s56 offen
	v_mbcnt_lo_u32_b32 v253, -1, 0
	v_mbcnt_hi_u32_b32 v253, -1, v253
	v_lshlrev_b32_e32 v253, 4, v253
	v_add_u32_e32 v253, s84, v253
	ds_read_b128 v[248:251], v253
	ds_read_b128 v[252:255], v253 offset:1024
	s_cmp_eq_u32 s27, 2
	s_cbranch_scc0 .Lka_nopub
	s_cmp_eq_u32 s50, 0
	s_cbranch_scc0 .Lf1_pub_done
	v_mov_b32_e32 v210, s70
	s_mov_b64 exec, 1
	global_store_dword v209, v210, s[72:73] offset:3072 sc1
	s_mov_b64 exec, -1

.Lka_single:
	v_cvt_pk_bf16_f32 v248, v248, v249
	v_cvt_pk_bf16_f32 v249, v250, v251
	v_cvt_pk_bf16_f32 v250, v252, v253
	v_cvt_pk_bf16_f32 v251, v254, v255
	v_lshrrev_b32_e32 v252, 1, v208
	buffer_store_dwordx4 v[248:251], v252, s[12:15], s56 offen
	s_nop 1
	global_load_dwordx4 v[248:251], v208, s[74:75] nt
	global_load_dwordx4 v[252:255], v208, s[74:75] offset:16 nt
	s_add_u32 s74, s74, 0x2000
	s_addc_u32 s75, s75, 0
.Lka_done:
	v_max3_f32 v156, v112, v113, v80
	v_max3_f32 v157, v114, v115, v81
	s_nop 0
	v_max3_f32 v156, v156, v82, v83
	v_mfma_f32_32x32x16_bf16 a[16:31], v[176:179], v[144:147], a[16:31]
	ds_read_b128 a[224:227], v217 offset:8192
	v_max3_f32 v156, v156, v116, v117
	v_max3_f32 v157, v157, v118, v119
	v_max3_f32 v156, v156, v84, v85
	v_max3_f32 v157, v157, v86, v87
	v_mfma_f32_32x32x16_bf16 a[32:47], v[168:171], v[128:131], a[32:47]
	ds_read_b128 a[228:231], v199 offset:8192
	v_max3_f32 v156, v156, v120, v121
	v_max3_f32 v157, v157, v122, v123
	v_max3_f32 v156, v156, v88, v89
	v_max3_f32 v157, v157, v90, v91
	v_mfma_f32_32x32x16_bf16 a[48:63], v[168:171], v[144:147], a[48:63]
	ds_read_b128 a[232:235], v198 offset:8192
	v_max3_f32 v156, v156, v124, v125
	v_max3_f32 v157, v157, v126, v127
	v_max3_f32 v156, v156, v92, v93
	v_max3_f32 v157, v157, v94, v95
	v_mfma_f32_32x32x16_bf16 a[64:79], v[160:163], v[128:131], a[64:79]
	ds_read_b128 a[236:239], v197 offset:8192
	v_max3_f32 v158, v96, v97, v64
	v_max3_f32 v159, v98, v99, v65
	v_max3_f32 v158, v158, v66, v67
	v_mfma_f32_32x32x16_bf16 a[80:95], v[160:163], v[144:147], a[80:95]
	ds_read_b128 a[240:243], v217 offset:8320
	v_max3_f32 v158, v158, v100, v101
	v_max3_f32 v159, v159, v102, v103
	v_max3_f32 v158, v158, v68, v69
	v_max3_f32 v159, v159, v70, v71
	v_mfma_f32_32x32x16_bf16 a[96:111], v[136:139], v[128:131], a[96:111]
	ds_read_b128 a[244:247], v199 offset:8320
	v_max3_f32 v128, v158, v104, v105
	v_max3_f32 v129, v159, v106, v107
	v_max3_f32 v128, v128, v72, v73
	v_max3_f32 v129, v129, v74, v75
	v_mfma_f32_32x32x16_bf16 a[112:127], v[136:139], v[144:147], a[112:127]
	ds_read_b128 a[248:251], v198 offset:8320
	v_max3_f32 v128, v128, v108, v109
	v_max3_f32 v129, v129, v110, v111
	v_max3_f32 v128, v128, v76, v77
	v_max3_f32 v130, v129, v78, v79
	v_mfma_f32_32x32x16_bf16 a[0:15], v[132:135], v[52:55], a[0:15]
	ds_read_b128 a[252:255], v197 offset:8320
	s_cmp_gt_u32 s27, 4
	s_cbranch_scc1 .Lkb2_done
	s_waitcnt lgkmcnt(8)
	v_pk_add_f32 v[200:201], v[248:249], v[200:201]
	v_pk_add_f32 v[202:203], v[250:251], v[202:203]
	v_pk_add_f32 v[204:205], v[252:253], v[204:205]
	v_pk_add_f32 v[206:207], v[254:255], v[206:207]
	v_cvt_pk_bf16_f32 v248, v248, v249
	v_cvt_pk_bf16_f32 v249, v250, v251
	v_cvt_pk_bf16_f32 v250, v252, v253
	v_cvt_pk_bf16_f32 v251, v254, v255
	v_lshrrev_b32_e32 v252, 1, v208
	buffer_store_dwordx4 v[248:251], v252, s[4:7], s56 offen
	s_add_i32 s56, s56, 0x1000
	s_nop 1
	global_load_dwordx4 v[248:251], v208, s[54:55] nt
	global_load_dwordx4 v[252:255], v208, s[54:55] offset:16 nt
	s_add_u32 s54, s54, 0x2000
	s_addc_u32 s55, s55, 0
	s_mov_b32 m0, s84
	s_nop 0
	buffer_load_dwordx4 v208, s[80:83], s86 offen lds
	s_mov_b32 m0, s85
	s_nop 0
	buffer_load_dwordx4 v208, s[80:83], s86 offen offset:16 lds
	s_add_i32 s86, s86, 0x2000

.LBB0_19:
	s_waitcnt lgkmcnt(0)
	v_mfma_f32_32x32x16_bf16 v[112:127], a[192:195], a[128:131], v[0:15]
	v_exp_f32_e32 v80, v80
	v_exp_f32_e32 v81, v81
	ds_read_b64_tr_b16 v[180:181], v212 offset:0
	v_cvt_pk_bf16_f32 v168, v128, v129
	v_exp_f32_e32 v82, v82
	v_exp_f32_e32 v83, v83
	v_mfma_f32_32x32x16_bf16 v[96:111], a[192:195], a[160:163], v[16:31]
	ds_read_b64_tr_b16 v[182:183], v212 offset:0x800
	v_cvt_pk_bf16_f32 v169, v130, v131
	v_mfma_f32_32x32x16_bf16 v[48:63], a[224:227], a[128:131], v[0:15]
	ds_read_b64_tr_b16 v[184:185], v212 offset:0x200
	v_exp_f32_e32 v239, v84
	v_exp_f32_e32 v240, v85
	v_cvt_pk_bf16_f32 v170, v132, v133
	v_mfma_f32_32x32x16_bf16 v[32:47], a[224:227], a[160:163], v[16:31]
	ds_read_b64_tr_b16 v[186:187], v212 offset:0xa00
	ds_read_b64_tr_b16 v[176:177], v212 offset:0x400
	v_exp_f32_e32 v241, v86
	v_exp_f32_e32 v242, v87
	v_cvt_pk_bf16_f32 v171, v134, v135
	v_exp_f32_e32 v227, v88
	v_exp_f32_e32 v228, v89
	v_mfma_f32_32x32x16_bf16 v[112:127], a[196:199], a[132:135], v[112:127]
	ds_read_b64_tr_b16 v[178:179], v212 offset:0xc00
	v_cvt_pk_bf16_f32 v128, v136, v137
	v_exp_f32_e32 v229, v90
	v_exp_f32_e32 v230, v91
	v_mfma_f32_32x32x16_bf16 v[96:111], a[196:199], a[164:167], v[96:111]
	ds_read_b64_tr_b16 v[188:189], v212 offset:0x600
	v_cvt_pk_bf16_f32 v129, v138, v139
	v_exp_f32_e32 v231, v92
	v_exp_f32_e32 v232, v93
	v_mfma_f32_32x32x16_bf16 v[48:63], a[228:231], a[132:135], v[48:63]
	ds_read_b64_tr_b16 v[190:191], v212 offset:0xe00
	v_cvt_pk_bf16_f32 v130, v140, v141
	v_mfma_f32_32x32x16_bf16 v[32:47], a[228:231], a[164:167], v[32:47]
	ds_read_b64_tr_b16 v[172:173], v212 offset:0x1000
	v_exp_f32_e32 v233, v94
	v_exp_f32_e32 v234, v95
	ds_read_b64_tr_b16 v[174:175], v212 offset:0x1800
	v_cvt_pk_bf16_f32 v131, v142, v143
	v_exp_f32_e32 v141, v64
	v_exp_f32_e32 v142, v65
	v_mfma_f32_32x32x16_bf16 v[112:127], a[200:203], a[136:139], v[112:127]
	ds_read_b64_tr_b16 v[164:165], v212 offset:0x1200
	v_cvt_pk_bf16_f32 v192, v144, v145
	v_exp_f32_e32 v143, v66
	v_mfma_f32_32x32x16_bf16 v[96:111], a[200:203], a[168:171], v[96:111]
	ds_read_b64_tr_b16 v[166:167], v212 offset:0x1a00
	v_exp_f32_e32 v243, v67
	v_cvt_pk_bf16_f32 v193, v146, v147
	v_mfma_f32_32x32x16_bf16 v[48:63], a[232:235], a[136:139], v[48:63]
	ds_read_b64_tr_b16 v[160:161], v212 offset:0x1400
	v_exp_f32_e32 v244, v68
	v_exp_f32_e32 v245, v69
	v_cvt_pk_bf16_f32 v194, v148, v149
	v_mfma_f32_32x32x16_bf16 v[32:47], a[232:235], a[168:171], v[32:47]
	ds_read_b64_tr_b16 v[162:163], v212 offset:0x1c00
	ds_read_b64_tr_b16 v[136:137], v212 offset:0x1600
	v_exp_f32_e32 v246, v70
	v_exp_f32_e32 v247, v71
	v_cvt_pk_bf16_f32 v195, v150, v151
	v_exp_f32_e32 v148, v72
	v_exp_f32_e32 v149, v73
	v_mfma_f32_32x32x16_bf16 v[112:127], a[204:207], a[140:143], v[112:127]
	ds_read_b64_tr_b16 v[138:139], v212 offset:0x1e00
	v_cvt_pk_bf16_f32 v144, v152, v153
	v_exp_f32_e32 v150, v74
	v_exp_f32_e32 v151, v75
	v_mfma_f32_32x32x16_bf16 v[96:111], a[204:207], a[172:175], v[96:111]
	ds_read_b64_tr_b16 v[132:133], v212 offset:0x2000
	v_cvt_pk_bf16_f32 v145, v154, v155
	v_exp_f32_e32 v152, v76
	v_exp_f32_e32 v153, v77
	v_mfma_f32_32x32x16_bf16 v[48:63], a[236:239], a[140:143], v[48:63]
	ds_read_b64_tr_b16 v[134:135], v212 offset:0x2800
	v_cvt_pk_bf16_f32 v146, v156, v157
	v_mfma_f32_32x32x16_bf16 v[32:47], a[236:239], a[172:175], v[32:47]
	ds_read_b64_tr_b16 v[92:93], v212 offset:0x2200
	v_exp_f32_e32 v154, v78
	v_exp_f32_e32 v155, v79
	ds_read_b64_tr_b16 v[94:95], v212 offset:0x2a00
	v_cvt_pk_bf16_f32 v147, v158, v159
	s_mov_b32 s0, s3
	v_mfma_f32_32x32x16_bf16 v[112:127], a[208:211], a[144:147], v[112:127]
	ds_read_b64_tr_b16 v[88:89], v212 offset:0x2400
	v_cvt_pk_bf16_f32 v84, v80, v81
	v_add_f32_e32 v64, v236, v80
	v_add_f32_e32 v65, v235, v81
	s_add_i32 s58, s57, s60
	s_and_b32 s58, s58, 0x7ffff
	s_mov_b32 s1, s58
	v_mfma_f32_32x32x16_bf16 v[96:111], a[208:211], a[176:179], v[96:111]
	ds_read_b64_tr_b16 v[90:91], v212 offset:0x2c00
	v_cvt_pk_bf16_f32 v85, v82, v83
	v_add_f32_e32 v64, v64, v82
	v_add_f32_e32 v65, v65, v83
	s_mov_b32 s35, s10
	v_mfma_f32_32x32x16_bf16 v[48:63], a[240:243], a[144:147], v[48:63]
	ds_read_b64_tr_b16 v[80:81], v212 offset:0x2600
	v_cvt_pk_bf16_f32 v86, v239, v240
	v_add_f32_e32 v64, v64, v239
	v_add_f32_e32 v65, v65, v240
	s_add_i32 s36, s58, 0x400
	v_mfma_f32_32x32x16_bf16 v[32:47], a[240:243], a[176:179], v[32:47]
	ds_read_b64_tr_b16 v[82:83], v212 offset:0x2e00
	ds_read_b64_tr_b16 v[76:77], v212 offset:0x3000
	v_cvt_pk_bf16_f32 v87, v241, v242
	v_add_f32_e32 v64, v64, v241
	v_add_f32_e32 v65, v65, v242
	s_mov_b32 s37, s11
	v_mfma_f32_32x32x16_bf16 v[112:127], a[212:215], a[148:151], v[112:127]
	ds_read_b64_tr_b16 v[78:79], v212 offset:0x3800
	v_add_f32_e32 v64, v64, v227
	v_add_f32_e32 v65, v65, v228
	s_add_i32 s38, s58, 0x800
	v_mfma_f32_32x32x16_bf16 v[96:111], a[212:215], a[180:183], v[96:111]
	ds_read_b64_tr_b16 v[72:73], v212 offset:0x3200
	v_add_f32_e32 v64, v64, v229
	v_add_f32_e32 v65, v65, v230
	s_mov_b32 s39, s16
	v_mfma_f32_32x32x16_bf16 v[48:63], a[244:247], a[148:151], v[48:63]
	ds_read_b64_tr_b16 v[74:75], v212 offset:0x3a00
	v_add_f32_e32 v64, v64, v231
	v_add_f32_e32 v65, v65, v232
	s_add_i32 s40, s58, 0xc00
	v_mfma_f32_32x32x16_bf16 v[32:47], a[244:247], a[180:183], v[32:47]
	ds_read_b64_tr_b16 v[68:69], v212 offset:0x3400
	ds_read_b64_tr_b16 v[70:71], v212 offset:0x3c00
	v_add_f32_e32 v156, v64, v233
	v_add_f32_e32 v157, v65, v234
	s_mov_b32 s41, s2
	v_mfma_f32_32x32x16_bf16 v[112:127], a[216:219], a[152:155], v[112:127]
	ds_read_b64_tr_b16 v[64:65], v212 offset:0x3600
	v_cvt_pk_bf16_f32 v140, v141, v142
	v_add_f32_e32 v158, v237, v141
	v_add_f32_e32 v142, v238, v142
	v_mfma_f32_32x32x16_bf16 v[96:111], a[216:219], a[184:187], v[96:111]
	ds_read_b64_tr_b16 v[66:67], v212 offset:0x3e00
	v_cvt_pk_bf16_f32 v141, v143, v243
	v_add_f32_e32 v143, v158, v143
	v_add_f32_e32 v158, v142, v243
	v_mfma_f32_32x32x16_bf16 v[48:63], a[248:251], a[152:155], v[48:63]
	s_mov_b32 s42, s17
	v_cvt_pk_bf16_f32 v142, v244, v245
	v_add_f32_e32 v159, v143, v244
	v_add_f32_e32 v158, v158, v245
	v_mfma_f32_32x32x16_bf16 v[32:47], a[248:251], a[184:187], v[32:47]
	s_add_i32 s43, s57, 0x80
	v_cvt_pk_bf16_f32 v143, v246, v247
	v_add_f32_e32 v159, v159, v246
	v_add_f32_e32 v158, v158, v247
	v_mfma_f32_32x32x16_bf16 v[112:127], a[220:223], a[156:159], v[112:127]
	s_mov_b32 s44, s18
	v_add_f32_e32 v159, v159, v148
	v_add_f32_e32 v158, v158, v149
	v_mfma_f32_32x32x16_bf16 v[96:111], a[220:223], a[188:191], v[96:111]
	v_add_f32_e32 v159, v159, v150
	v_add_f32_e32 v158, v158, v151
	v_mfma_f32_32x32x16_bf16 v[48:63], a[252:255], a[156:159], v[48:63]
	s_mov_b32 s45, s19
	v_add_f32_e32 v159, v159, v152
	v_add_f32_e32 v158, v158, v153
	v_mfma_f32_32x32x16_bf16 v[32:47], a[252:255], a[188:191], v[32:47]
	s_add_i32 s46, s57, 0x880
	v_add_f32_e32 v159, v159, v154
	v_add_f32_e32 v158, v158, v155
	v_add_f32_e32 v156, v156, v157
	s_waitcnt vmcnt(0) lgkmcnt(0)
	s_barrier
	s_mov_b32 m0, s0
	v_mfma_f32_32x32x16_bf16 a[0:15], v[180:183], v[168:171], a[0:15]
	buffer_load_dwordx4 v222, s[12:15], s1 offen lds
	s_mov_b32 m0, s35
	v_mfma_f32_32x32x16_bf16 a[16:31], v[180:183], v[192:195], a[16:31]
	buffer_load_dwordx4 v223, s[12:15], s36 offen lds
	ds_read_b128 a[192:195], v218 offset:0
	s_mov_b32 m0, s37
	v_mfma_f32_32x32x16_bf16 a[32:47], v[184:187], v[168:171], a[32:47]
	v_add_f32_e32 v225, v225, v156
	v_add_f32_e32 v156, v159, v158
	buffer_load_dwordx4 v222, s[12:15], s38 offen lds
	ds_read_b128 a[196:199], v219 offset:0
	s_mov_b32 m0, s39
	v_mfma_f32_32x32x16_bf16 a[48:63], v[184:187], v[192:195], a[48:63]
	buffer_load_dwordx4 v223, s[12:15], s40 offen lds
	ds_read_b128 a[200:203], v220 offset:0
	s_mov_b32 m0, s41
	v_mfma_f32_32x32x16_bf16 a[64:79], v[176:179], v[168:171], a[64:79]
	v_add_f32_e32 v226, v226, v156
	buffer_load_dwordx4 v196, s[4:7], s33 offen lds
	ds_read_b128 a[204:207], v221 offset:0
	s_mov_b32 m0, s42
	v_mfma_f32_32x32x16_bf16 a[80:95], v[176:179], v[192:195], a[80:95]
	buffer_load_dwordx4 v196, s[4:7], s43 offen lds
	ds_read_b128 a[208:211], v218 offset:128
	s_mov_b32 m0, s44
	v_mfma_f32_32x32x16_bf16 a[96:111], v[188:191], v[168:171], a[96:111]
	buffer_load_dwordx4 v196, s[4:7], s34 offen lds
	ds_read_b128 a[212:215], v219 offset:128
	s_mov_b32 m0, s45
	v_mfma_f32_32x32x16_bf16 a[112:127], v[188:191], v[192:195], a[112:127]
	buffer_load_dwordx4 v196, s[4:7], s46 offen lds
	ds_read_b128 a[216:219], v220 offset:128
	s_nop 0
	v_mfma_f32_32x32x16_bf16 a[0:15], v[172:175], v[128:131], a[0:15]
	ds_read_b128 a[220:223], v221 offset:128
	s_cmp_gt_u32 s27, 12
	s_cbranch_scc1 .Lkc_done
	s_cmp_gt_u32 s27, 4
	s_cbranch_scc1 .Lkc_single
	v_cvt_pk_bf16_f32 v248, v248, v249
	v_cvt_pk_bf16_f32 v249, v250, v251
	v_cvt_pk_bf16_f32 v250, v252, v253
	v_cvt_pk_bf16_f32 v251, v254, v255
	v_lshrrev_b32_e32 v252, 1, v208
	buffer_store_dwordx4 v[248:251], v252, s[12:15], s56 offen
	v_mbcnt_lo_u32_b32 v253, -1, 0
	v_mbcnt_hi_u32_b32 v253, -1, v253
	v_lshlrev_b32_e32 v253, 4, v253
	v_add_u32_e32 v253, s84, v253
	ds_read_b128 v[248:251], v253
	ds_read_b128 v[252:255], v253 offset:1024
	s_branch .Lkc_done
.Lkc_single:
	v_pk_add_f32 v[200:201], v[248:249], v[200:201]
	v_pk_add_f32 v[202:203], v[250:251], v[202:203]
	v_pk_add_f32 v[204:205], v[252:253], v[204:205]
	v_pk_add_f32 v[206:207], v[254:255], v[206:207]
	v_cvt_pk_bf16_f32 v248, v248, v249
	v_cvt_pk_bf16_f32 v249, v250, v251
	v_cvt_pk_bf16_f32 v250, v252, v253
	v_cvt_pk_bf16_f32 v251, v254, v255
	v_lshrrev_b32_e32 v252, 1, v208
	buffer_store_dwordx4 v[248:251], v252, s[4:7], s56 offen
	s_add_i32 s56, s56, 0x1000
	s_cmp_gt_u32 s27, 10
	s_cbranch_scc1 .Lkc_done
	s_nop 1
	global_load_dwordx4 v[248:251], v208, s[54:55] nt
	global_load_dwordx4 v[252:255], v208, s[54:55] offset:16 nt
	s_add_u32 s54, s54, 0x2000
	s_addc_u32 s55, s55, 0
.Lkc_done:
	v_max3_f32 v156, v112, v113, v48
	v_max3_f32 v157, v114, v115, v49
	s_nop 0
	v_max3_f32 v156, v156, v50, v51
	v_mfma_f32_32x32x16_bf16 a[16:31], v[172:175], v[144:147], a[16:31]
	ds_read_b128 a[224:227], v218 offset:8192
	v_max3_f32 v156, v156, v116, v117
	v_max3_f32 v157, v157, v118, v119
	v_max3_f32 v156, v156, v52, v53
	v_max3_f32 v157, v157, v54, v55
	v_mfma_f32_32x32x16_bf16 a[32:47], v[164:167], v[128:131], a[32:47]
	ds_read_b128 a[228:231], v219 offset:8192
	v_max3_f32 v156, v156, v120, v121
	v_max3_f32 v157, v157, v122, v123
	v_max3_f32 v156, v156, v56, v57
	v_max3_f32 v157, v157, v58, v59
	v_mfma_f32_32x32x16_bf16 a[48:63], v[164:167], v[144:147], a[48:63]
	ds_read_b128 a[232:235], v220 offset:8192
	v_max3_f32 v156, v156, v124, v125
	v_max3_f32 v157, v157, v126, v127
	v_max3_f32 v156, v156, v60, v61
	v_max3_f32 v157, v157, v62, v63
	v_mfma_f32_32x32x16_bf16 a[64:79], v[160:163], v[128:131], a[64:79]
	ds_read_b128 a[236:239], v221 offset:8192
	v_max3_f32 v158, v96, v97, v32
	v_max3_f32 v159, v98, v99, v33
	v_max3_f32 v158, v158, v34, v35
	v_mfma_f32_32x32x16_bf16 a[80:95], v[160:163], v[144:147], a[80:95]
	ds_read_b128 a[240:243], v218 offset:8320
	v_max3_f32 v158, v158, v100, v101
	v_max3_f32 v159, v159, v102, v103
	v_max3_f32 v158, v158, v36, v37
	v_max3_f32 v159, v159, v38, v39
	v_mfma_f32_32x32x16_bf16 a[96:111], v[136:139], v[128:131], a[96:111]
	ds_read_b128 a[244:247], v219 offset:8320
	v_max3_f32 v128, v158, v104, v105
	v_max3_f32 v129, v159, v106, v107
	v_max3_f32 v128, v128, v40, v41
	v_max3_f32 v129, v129, v42, v43
	v_mfma_f32_32x32x16_bf16 a[112:127], v[136:139], v[144:147], a[112:127]
	ds_read_b128 a[248:251], v220 offset:8320
	v_max3_f32 v128, v128, v108, v109
	v_max3_f32 v129, v129, v110, v111
	v_max3_f32 v128, v128, v44, v45
	v_max3_f32 v130, v129, v46, v47
	v_mfma_f32_32x32x16_bf16 a[0:15], v[132:135], v[84:87], a[0:15]
	ds_read_b128 a[252:255], v221 offset:8320
	s_cmp_gt_u32 s27, 4
	s_cbranch_scc1 .Lkd2_done
	s_waitcnt lgkmcnt(8)
	v_pk_add_f32 v[200:201], v[248:249], v[200:201]
	v_pk_add_f32 v[202:203], v[250:251], v[202:203]
	v_pk_add_f32 v[204:205], v[252:253], v[204:205]
	v_pk_add_f32 v[206:207], v[254:255], v[206:207]
	v_cvt_pk_bf16_f32 v248, v248, v249
	v_cvt_pk_bf16_f32 v249, v250, v251
	v_cvt_pk_bf16_f32 v250, v252, v253
	v_cvt_pk_bf16_f32 v251, v254, v255
	v_lshrrev_b32_e32 v252, 1, v208
	buffer_store_dwordx4 v[248:251], v252, s[4:7], s56 offen
	s_add_i32 s56, s56, 0x1000
	s_nop 1
	global_load_dwordx4 v[248:251], v208, s[54:55] nt
	global_load_dwordx4 v[252:255], v208, s[54:55] offset:16 nt
	s_add_u32 s54, s54, 0x2000
	s_addc_u32 s55, s55, 0
	s_cmp_gt_u32 s27, 2
	s_cbranch_scc1 .Lkd2_done
	s_mov_b32 m0, s84
	s_nop 0
	buffer_load_dwordx4 v208, s[80:83], s86 offen lds
	s_mov_b32 m0, s85
	s_nop 0
	buffer_load_dwordx4 v208, s[80:83], s86 offen offset:16 lds
	s_add_i32 s86, s86, 0x2000
